# scan elementwise waves: transposed LDS reads of the staged chunk issued at the end of the preceding idle step
# speedup vs baseline: 1.0046x; 1.0046x over previous
.LBB0_948:
	s_cmp_lt_u32 s67, 64
	s_cselect_b64 vcc, -1, 0
	v_cndmask_b32_e32 v0, v130, v126, vcc
	v_or_b32_e32 v4, s20, v0
	v_cndmask_b32_e32 v0, v131, v132, vcc
	v_or_b32_e32 v6, s20, v0
	v_lshlrev_b32_e32 v0, 13, v4
	v_lshl_add_u64 v[2:3], s[86:87], 0, v[0:1]
	s_lshl_b32 s8, s12, 7
	s_mov_b32 s9, s21
	v_lshl_add_u64 v[2:3], v[2:3], 0, s[8:9]
	v_mov_b32_e32 v115, v1
	v_lshlrev_b32_e32 v0, 13, v6
	v_lshl_add_u64 v[18:19], v[2:3], 0, v[114:115]
	v_lshl_add_u64 v[2:3], s[86:87], 0, v[0:1]
	v_lshl_add_u64 v[2:3], v[2:3], 0, s[8:9]
	v_lshl_add_u64 v[22:23], v[2:3], 0, v[114:115]
	v_mov_b64_e32 v[2:3], s[88:89]
	s_movk_i32 s5, 0x2800
	v_mad_u64_u32 v[4:5], s[6:7], v4, s5, v[2:3]
	s_lshl_b32 s6, s4, 10
	s_ashr_i32 s7, s6, 31
	s_lshl_b64 s[10:11], s[6:7], 1
	v_mad_u64_u32 v[2:3], s[60:61], v6, s5, v[2:3]
	v_lshl_add_u64 v[4:5], v[4:5], 0, s[10:11]
	v_lshl_add_u64 v[2:3], v[2:3], 0, s[10:11]
	s_movk_i32 s5, 0x1000
	v_lshl_add_u64 v[4:5], v[4:5], 0, s[8:9]
	v_lshl_add_u64 v[2:3], v[2:3], 0, s[8:9]
	v_add_co_u32_e32 v10, vcc, s5, v18
	v_lshl_add_u64 v[20:21], v[4:5], 0, v[114:115]
	v_lshl_add_u64 v[24:25], v[2:3], 0, v[114:115]
	v_addc_co_u32_e32 v11, vcc, 0, v19, vcc
	global_load_dwordx4 v[2:5], v[20:21], off nt
	global_load_dwordx4 v[6:9], v[24:25], off nt
	v_add_co_u32_e32 v14, vcc, s5, v22
	v_lshl_add_u64 v[20:21], v[20:21], 0, s[14:15]
	v_lshl_add_u64 v[24:25], v[24:25], 0, s[14:15]
	v_addc_co_u32_e32 v15, vcc, 0, v23, vcc
	v_cndmask_b32_e64 v27, v25, v23, s[38:39]
	v_cndmask_b32_e64 v26, v24, v22, s[38:39]
	v_cndmask_b32_e64 v25, v21, v19, s[38:39]
	v_cndmask_b32_e64 v24, v20, v18, s[38:39]
	v_lshl_add_u64 v[18:19], v[18:19], 0, s[92:93]
	v_lshl_add_u64 v[30:31], v[22:23], 0, s[92:93]
	global_load_dwordx4 v[10:13], v[10:11], off offset:2048 nt
	s_nop 0
	global_load_dwordx4 v[14:17], v[14:15], off offset:2048 nt
	s_lshl_b32 s8, s12, 6
	global_load_dwordx4 v[18:21], v[18:19], off nt
	s_nop 0
	global_load_dwordx4 v[22:25], v[24:25], off nt
	s_nop 0
	global_load_dwordx4 v[26:29], v[26:27], off nt
	s_nop 0
	global_load_dwordx4 v[30:33], v[30:31], off nt
	s_waitcnt vmcnt(0)
	s_waitcnt vmcnt(7)
	ds_write_b128 v151, v[2:5]
	s_waitcnt vmcnt(6)
	ds_write_b128 v151, v[6:9] offset:1024
	s_waitcnt vmcnt(5)
	ds_write_b128 v151, v[10:13] offset:2048
	s_waitcnt vmcnt(3)
	ds_write_b128 v151, v[18:21] offset:6144
	ds_write_b128 v151, v[14:17] offset:3072
	s_waitcnt vmcnt(2)
	ds_write_b128 v151, v[22:25] offset:4096
	s_waitcnt vmcnt(1)
	ds_write_b128 v151, v[26:29] offset:5120
	s_waitcnt vmcnt(0)
	ds_write_b128 v151, v[30:33] offset:7168
	v_add_u32_e32 v208, s29, v129
	ds_read_b64_tr_b16 v[176:177], v208
	ds_read_b64_tr_b16 v[178:179], v208 offset:512
	ds_read_b64_tr_b16 v[180:181], v208 offset:1024
	ds_read_b64_tr_b16 v[182:183], v208 offset:1536
	ds_read_b64_tr_b16 v[184:185], v208 offset:2048
	ds_read_b64_tr_b16 v[186:187], v208 offset:2560
	ds_read_b64_tr_b16 v[188:189], v208 offset:3072
	ds_read_b64_tr_b16 v[190:191], v208 offset:3584
	ds_read_b64_tr_b16 v[192:193], v208 offset:4096
	ds_read_b64_tr_b16 v[194:195], v208 offset:4608
	ds_read_b64_tr_b16 v[196:197], v208 offset:5120
	ds_read_b64_tr_b16 v[198:199], v208 offset:5632
	ds_read_b64_tr_b16 v[200:201], v208 offset:6144
	ds_read_b64_tr_b16 v[202:203], v208 offset:6656
	ds_read_b64_tr_b16 v[204:205], v208 offset:7168
	ds_read_b64_tr_b16 v[206:207], v208 offset:7680
	s_waitcnt lgkmcnt(0)

.LBB0_959:
	s_and_b64 vcc, exec, s[12:13]
	s_cbranch_vccz .LBB0_968
	s_and_b32 s10, s84, 1
	v_cndmask_b32_e64 v0, 0, 1, s[90:91]
	v_cmp_eq_u32_e32 vcc, s10, v0
	s_mov_b64 s[10:11], -1
	s_cbranch_vccz .LBB0_964
	s_cmpk_gt_u32 s84, 0xff
	s_cbranch_scc1 .LBB0_963
	v_add_u32_e32 v58, s29, v129
	s_mul_i32 s10, s84, 0xab
	s_waitcnt lgkmcnt(3)
	v_and_b32_e32 v60, 0xffff0000, v176
	v_lshlrev_b32_e32 v61, 16, v176
	v_lshlrev_b32_e32 v62, 16, v177
	v_and_b32_e32 v63, 0xffff0000, v177
	s_waitcnt lgkmcnt(2)
	v_lshlrev_b32_e32 v64, 16, v192
	v_and_b32_e32 v66, 0xffff0000, v192
	v_lshlrev_b32_e32 v68, 16, v193
	v_and_b32_e32 v70, 0xffff0000, v193
	s_waitcnt lgkmcnt(0)
	v_lshlrev_b32_e32 v72, 16, v200
	v_and_b32_e32 v73, 0xffff0000, v200
	v_lshlrev_b32_e32 v74, 16, v201
	v_and_b32_e32 v75, 0xffff0000, v201
	s_bfe_u32 s10, s10, 0x70009
	s_mul_i32 s10, s10, 3
	v_mul_f32_e32 v60, v60, v61
	s_sub_i32 s10, s84, s10
	v_lshlrev_b32_e32 v65, 16, v184
	v_and_b32_e32 v67, 0xffff0000, v184
	s_waitcnt lgkmcnt(3)
	v_lshlrev_b32_e32 v76, 16, v178
	v_and_b32_e32 v77, 0xffff0000, v178
	v_lshlrev_b32_e32 v78, 16, v179
	v_and_b32_e32 v12, 0xffff0000, v179
	s_waitcnt lgkmcnt(0)
	v_lshlrev_b32_e32 v83, 16, v202
	v_and_b32_e32 v84, 0xffff0000, v202
	v_lshlrev_b32_e32 v51, 16, v203
	v_and_b32_e32 v11, 0xffff0000, v203
	v_rcp_f32_e32 v97, v61
	v_rcp_f32_e32 v61, v60
	s_and_b32 s10, s10, 0xff
	v_mul_f32_e32 v65, v65, v64
	v_add_f32_e32 v64, -1.0, v64
	v_mul_f32_e32 v67, v67, v66
	v_add_f32_e32 v66, -1.0, v66
	s_mulk_i32 s10, 0x5300
	s_waitcnt vmcnt(0)
	v_fma_f32 v64, v152, v64, 1.0
	v_fma_f32 v66, v152, v66, 1.0
	s_add_i32 s10, s10, 0
	v_mul_f32_e32 v64, v64, v72
	v_mul_f32_e32 v66, v66, v73
	v_mul_f32_e32 v60, v60, v62
	v_lshlrev_b32_e32 v69, 16, v185
	v_mul_f32_e32 v65, v97, v65
	v_mul_f32_e32 v64, v97, v64
	v_cvt_pk_bf16_f32 v72, v65, v64
	v_add_u32_e32 v97, s10, v127
	v_mul_f32_e32 v67, v61, v67
	v_mul_f32_e32 v61, v61, v66
	v_cvt_pk_bf16_f32 v66, v67, v61
	v_rcp_f32_e32 v62, v60
	v_and_b32_e32 v71, 0xffff0000, v185
	v_lshlrev_b32_e32 v79, 16, v194
	v_lshlrev_b32_e32 v80, 16, v186
	v_and_b32_e32 v81, 0xffff0000, v194
	v_and_b32_e32 v82, 0xffff0000, v186
	v_lshlrev_b32_e32 v15, 16, v195
	v_lshlrev_b32_e32 v49, 16, v187
	v_and_b32_e32 v7, 0xffff0000, v195
	v_and_b32_e32 v10, 0xffff0000, v187
	s_waitcnt lgkmcnt(3)
	v_lshlrev_b32_e32 v85, 16, v180
	v_and_b32_e32 v50, 0xffff0000, v180
	v_lshlrev_b32_e32 v9, 16, v181
	v_and_b32_e32 v4, 0xffff0000, v181
	s_waitcnt lgkmcnt(2)
	v_lshlrev_b32_e32 v86, 16, v196
	s_waitcnt lgkmcnt(1)
	v_lshlrev_b32_e32 v87, 16, v188
	v_and_b32_e32 v13, 0xffff0000, v196
	v_and_b32_e32 v14, 0xffff0000, v188
	v_lshlrev_b32_e32 v5, 16, v197
	v_lshlrev_b32_e32 v6, 16, v189
	v_and_b32_e32 v0, 0xffff0000, v197
	v_and_b32_e32 v2, 0xffff0000, v189
	s_waitcnt lgkmcnt(0)
	v_lshlrev_b32_e32 v88, 16, v204
	v_and_b32_e32 v48, 0xffff0000, v204
	v_lshlrev_b32_e32 v8, 16, v205
	v_and_b32_e32 v3, 0xffff0000, v205
	ds_write_b16 v97, v72 offset:5632
	ds_write_b16_d16_hi v97, v72 offset:7936
	ds_write_b16 v97, v66 offset:5776
	ds_write_b16_d16_hi v97, v66 offset:8080
	v_mul_f32_e32 v66, v69, v68
	v_add_f32_e32 v68, -1.0, v68
	v_mul_f32_e32 v60, v60, v63
	v_fma_f32 v68, v152, v68, 1.0
	v_rcp_f32_e32 v63, v60
	v_mul_f32_e32 v68, v68, v74
	v_add_f32_e32 v69, -1.0, v70
	v_mul_f32_e32 v66, v62, v66
	v_mul_f32_e32 v62, v62, v68
	v_cvt_pk_bf16_f32 v68, v66, v62
	v_fma_f32 v69, v152, v69, 1.0
	ds_write_b16 v97, v68 offset:5920
	ds_write_b16_d16_hi v97, v68 offset:8224
	v_mul_f32_e32 v68, v71, v70
	v_mul_f32_e32 v69, v69, v75
	v_mul_f32_e32 v68, v68, v63
	v_mul_f32_e32 v63, v63, v69
	v_cvt_pk_bf16_f32 v69, v68, v63
	v_mul_f32_e32 v60, v60, v76
	ds_write_b16 v97, v69 offset:6064
	ds_write_b16_d16_hi v97, v69 offset:8368
	v_rcp_f32_e32 v69, v60
	v_add_f32_e32 v71, -1.0, v79
	v_fma_f32 v71, v152, v71, 1.0
	v_mul_f32_e32 v70, v80, v79
	v_mul_f32_e32 v71, v71, v83
	v_mul_f32_e32 v70, v69, v70
	v_mul_f32_e32 v69, v69, v71
	v_cvt_pk_bf16_f32 v71, v70, v69
	v_mul_f32_e32 v60, v60, v77
	ds_write_b16 v97, v71 offset:6208
	ds_write_b16_d16_hi v97, v71 offset:8512
	v_rcp_f32_e32 v71, v60
	v_add_f32_e32 v73, -1.0, v81
	v_fma_f32 v73, v152, v73, 1.0
	v_mul_f32_e32 v72, v82, v81
	v_mul_f32_e32 v73, v73, v84
	v_mul_f32_e32 v72, v71, v72
	v_mul_f32_e32 v71, v71, v73
	v_cvt_pk_bf16_f32 v73, v72, v71
	v_mul_f32_e32 v60, v60, v78
	ds_write_b16 v97, v73 offset:6352
	ds_write_b16_d16_hi v97, v73 offset:8656
	v_rcp_f32_e32 v73, v60
	v_mul_f32_e32 v49, v49, v15
	v_add_f32_e32 v15, -1.0, v15
	v_fma_f32 v15, v152, v15, 1.0
	v_mul_f32_e32 v15, v15, v51
	v_mul_f32_e32 v49, v49, v73
	v_mul_f32_e32 v15, v73, v15
	v_cvt_pk_bf16_f32 v51, v49, v15
	v_mul_f32_e32 v12, v60, v12
	ds_write_b16 v97, v51 offset:6496
	ds_write_b16_d16_hi v97, v51 offset:8800
	v_rcp_f32_e32 v51, v12
	v_mul_f32_e32 v10, v10, v7
	v_add_f32_e32 v7, -1.0, v7
	v_fma_f32 v7, v152, v7, 1.0
	v_mul_f32_e32 v7, v7, v11
	v_mul_f32_e32 v10, v10, v51
	v_mul_f32_e32 v7, v51, v7
	v_cvt_pk_bf16_f32 v11, v10, v7
	ds_write_b16 v97, v11 offset:6640
	ds_write_b16_d16_hi v97, v11 offset:8944
	v_mul_f32_e32 v11, v12, v85
	v_rcp_f32_e32 v12, v11
	v_mul_f32_e32 v11, v11, v50
	v_mul_f32_e32 v9, v11, v9
	v_rcp_f32_e32 v50, v11
	v_rcp_f32_e32 v11, v9
	v_add_f32_e32 v60, -1.0, v86
	v_mul_f32_e32 v14, v14, v13
	v_add_f32_e32 v13, -1.0, v13
	v_mul_f32_e32 v6, v6, v5
	v_add_f32_e32 v5, -1.0, v5
	v_fma_f32 v60, v152, v60, 1.0
	v_fma_f32 v13, v152, v13, 1.0
	v_fma_f32 v5, v152, v5, 1.0
	v_mul_f32_e32 v51, v87, v86
	v_mul_f32_e32 v60, v60, v88
	v_mul_f32_e32 v13, v13, v48
	v_mul_f32_e32 v5, v5, v8
	v_mul_f32_e32 v51, v12, v51
	v_mul_f32_e32 v12, v12, v60
	v_cvt_pk_bf16_f32 v60, v51, v12
	v_mul_f32_e32 v14, v50, v14
	v_mul_f32_e32 v13, v50, v13
	v_cvt_pk_bf16_f32 v48, v14, v13
	v_mul_f32_e32 v6, v6, v11
	v_mul_f32_e32 v8, v11, v5
	v_cvt_pk_bf16_f32 v5, v6, v8
	v_mul_f32_e32 v4, v9, v4
	ds_write_b16 v97, v60 offset:6784
	ds_write_b16_d16_hi v97, v60 offset:9088
	ds_write_b16 v97, v48 offset:6928
	ds_write_b16_d16_hi v97, v48 offset:9232
	ds_write_b16 v97, v5 offset:7072
	ds_write_b16_d16_hi v97, v5 offset:9376
	v_rcp_f32_e32 v5, v4
	v_mul_f32_e32 v2, v2, v0
	v_add_f32_e32 v0, -1.0, v0
	v_fma_f32 v0, v152, v0, 1.0
	v_mul_f32_e32 v0, v0, v3
	s_waitcnt lgkmcnt(14)
	v_lshlrev_b32_e32 v89, 16, v182
	v_mul_f32_e32 v9, v2, v5
	v_mul_f32_e32 v0, v5, v0
	v_cvt_pk_bf16_f32 v2, v9, v0
	ds_write_b16 v97, v2 offset:7216
	ds_write_b16_d16_hi v97, v2 offset:9520
	v_mul_f32_e32 v2, v4, v89
	v_rcp_f32_e32 v3, v2
	v_lshlrev_b32_e32 v91, 16, v198
	v_lshlrev_b32_e32 v92, 16, v190
	v_mul_f32_e32 v4, v92, v91
	v_mul_f32_e32 v11, v3, v4
	v_add_f32_e32 v4, -1.0, v91
	v_lshlrev_b32_e32 v95, 16, v206
	v_fma_f32 v4, v152, v4, 1.0
	v_and_b32_e32 v52, 0xffff0000, v182
	v_mul_f32_e32 v4, v4, v95
	v_mul_f32_e32 v48, v3, v4
	v_cvt_pk_bf16_f32 v3, v11, v48
	v_mul_f32_e32 v2, v2, v52
	ds_write_b16 v97, v3 offset:7360
	ds_write_b16_d16_hi v97, v3 offset:9664
	v_rcp_f32_e32 v3, v2
	v_and_b32_e32 v54, 0xffff0000, v198
	v_and_b32_e32 v56, 0xffff0000, v190
	v_mul_f32_e32 v4, v56, v54
	v_mul_f32_e32 v50, v3, v4
	v_add_f32_e32 v4, -1.0, v54
	v_and_b32_e32 v58, 0xffff0000, v206
	v_fma_f32 v4, v152, v4, 1.0
	v_lshlrev_b32_e32 v90, 16, v183
	v_mul_f32_e32 v4, v4, v58
	v_mul_f32_e32 v52, v3, v4
	v_cvt_pk_bf16_f32 v3, v50, v52
	v_mul_f32_e32 v2, v2, v90
	ds_write_b16 v97, v3 offset:7504
	ds_write_b16_d16_hi v97, v3 offset:9808
	v_rcp_f32_e32 v3, v2
	v_lshlrev_b32_e32 v93, 16, v199
	v_lshlrev_b32_e32 v94, 16, v191
	v_and_b32_e32 v53, 0xffff0000, v183
	v_mul_f32_e32 v4, v94, v93
	v_mul_f32_e32 v54, v4, v3
	v_add_f32_e32 v4, -1.0, v93
	v_mul_f32_e32 v2, v2, v53
	v_lshlrev_b32_e32 v96, 16, v207
	v_fma_f32 v4, v152, v4, 1.0
	v_rcp_f32_e32 v2, v2
	v_mul_f32_e32 v4, v4, v96
	v_and_b32_e32 v55, 0xffff0000, v199
	v_and_b32_e32 v57, 0xffff0000, v191
	v_mul_f32_e32 v56, v3, v4
	v_cvt_pk_bf16_f32 v3, v54, v56
	ds_write_b16 v97, v3 offset:7648
	ds_write_b16_d16_hi v97, v3 offset:9952
	v_mul_f32_e32 v3, v57, v55
	v_mul_f32_e32 v53, v3, v2
	v_add_f32_e32 v3, -1.0, v55
	v_and_b32_e32 v59, 0xffff0000, v207
	v_fma_f32 v3, v152, v3, 1.0
	v_mul_f32_e32 v3, v3, v59
	v_mul_f32_e32 v55, v2, v3
	v_cvt_pk_bf16_f32 v2, v53, v55
	ds_write_b16 v97, v2 offset:7792
	ds_write_b16_d16_hi v97, v2 offset:10096
	v_add_u32_e32 v57, s10, v133
	v_cvt_pk_bf16_f32 v2, v65, v67
	v_cvt_pk_bf16_f32 v3, v66, v68
	v_cvt_pk_bf16_f32 v4, v70, v72
	v_cvt_pk_bf16_f32 v5, v49, v10
	ds_write_b128 v57, v[2:5] offset:10240
	v_cvt_pk_bf16_f32 v2, v51, v14
	v_cvt_pk_bf16_f32 v3, v6, v9
	v_cvt_pk_bf16_f32 v4, v11, v50
	v_cvt_pk_bf16_f32 v5, v54, v53
	ds_write_b128 v57, v[2:5] offset:10256
	v_cvt_pk_bf16_f32 v2, v64, v61
	v_cvt_pk_bf16_f32 v3, v62, v63
	v_cvt_pk_bf16_f32 v4, v69, v71
	v_cvt_pk_bf16_f32 v5, v15, v7
	ds_write_b128 v57, v[2:5] offset:10272
	v_cvt_pk_bf16_f32 v2, v12, v13
	v_cvt_pk_bf16_f32 v3, v8, v0
	v_cvt_pk_bf16_f32 v4, v48, v52
	v_cvt_pk_bf16_f32 v5, v56, v55
	ds_write_b128 v57, v[2:5] offset:10288

.LBB0_964:
	s_andn2_b64 vcc, exec, s[10:11]
	s_cbranch_vccnz .LBB0_967
	s_cmpk_gt_u32 s84, 0xfe
	s_cbranch_scc1 .LBB0_967
	v_add_u32_e32 v2, s70, v126
	v_add_u32_e32 v0, 16, v2
	v_add_u32_e32 v2, 24, v2
	v_cndmask_b32_e64 v0, v115, v0, s[60:61]
	v_cndmask_b32_e64 v2, v117, v2, s[60:61]
	v_add_u32_e32 v0, s20, v0
	v_add_u32_e32 v2, s20, v2
	s_movk_i32 s12, 0x2800
	v_lshlrev_b64 v[4:5], 13, v[0:1]
	v_mad_u64_u32 v[56:57], s[10:11], v0, s12, v[120:121]
	v_mad_u64_u32 v[58:59], s[10:11], v2, s12, v[120:121]
	v_mov_b32_e32 v3, v1
	v_lshl_add_u64 v[14:15], v[118:119], 0, v[4:5]
	s_movk_i32 s10, 0x1000
	v_lshlrev_b64 v[4:5], 13, v[2:3]
	v_add_co_u32_e32 v10, vcc, s10, v14
	v_lshl_add_u64 v[64:65], v[118:119], 0, v[4:5]
	s_nop 0
	v_addc_co_u32_e32 v11, vcc, 0, v15, vcc
	v_add_co_u32_e32 v48, vcc, s10, v64
	global_load_dwordx4 v[2:5], v[56:57], off nt
	global_load_dwordx4 v[6:9], v[58:59], off nt
	v_addc_co_u32_e32 v49, vcc, 0, v65, vcc
	global_load_dwordx4 v[10:13], v[10:11], off offset:2048 nt
	s_nop 0
	global_load_dwordx4 v[48:51], v[48:49], off offset:2048 nt
	s_nop 0
	global_load_dwordx4 v[52:55], v[14:15], off offset:2048 nt
	v_add_co_u32_e32 v14, vcc, s10, v58
	s_nop 1
	v_addc_co_u32_e32 v15, vcc, 0, v59, vcc
	v_add_co_u32_e32 v60, vcc, 0x1000, v56
	s_nop 1
	v_addc_co_u32_e32 v61, vcc, 0, v57, vcc
	global_load_dwordx4 v[56:59], v[14:15], off nt
	s_nop 0
	global_load_dwordx4 v[60:63], v[60:61], off nt
	s_nop 0
	global_load_dwordx4 v[64:67], v[64:65], off offset:2048 nt
	s_waitcnt vmcnt(0)
	s_waitcnt vmcnt(7)
	ds_write_b128 v151, v[2:5]
	s_waitcnt vmcnt(6)
	ds_write_b128 v151, v[6:9] offset:1024
	s_waitcnt vmcnt(3)
	ds_write_b128 v151, v[52:55] offset:6144
	ds_write_b128 v151, v[10:13] offset:2048
	ds_write_b128 v151, v[48:51] offset:3072
	s_waitcnt vmcnt(2)
	ds_write_b128 v151, v[56:59] offset:5120
	s_waitcnt vmcnt(1)
	ds_write_b128 v151, v[60:63] offset:4096
	s_waitcnt vmcnt(0)
	ds_write_b128 v151, v[64:67] offset:7168
	v_add_u32_e32 v208, s29, v129
	ds_read_b64_tr_b16 v[176:177], v208
	ds_read_b64_tr_b16 v[178:179], v208 offset:512
	ds_read_b64_tr_b16 v[180:181], v208 offset:1024
	ds_read_b64_tr_b16 v[182:183], v208 offset:1536
	ds_read_b64_tr_b16 v[184:185], v208 offset:2048
	ds_read_b64_tr_b16 v[186:187], v208 offset:2560
	ds_read_b64_tr_b16 v[188:189], v208 offset:3072
	ds_read_b64_tr_b16 v[190:191], v208 offset:3584
	ds_read_b64_tr_b16 v[192:193], v208 offset:4096
	ds_read_b64_tr_b16 v[194:195], v208 offset:4608
	ds_read_b64_tr_b16 v[196:197], v208 offset:5120
	ds_read_b64_tr_b16 v[198:199], v208 offset:5632
	ds_read_b64_tr_b16 v[200:201], v208 offset:6144
	ds_read_b64_tr_b16 v[202:203], v208 offset:6656
	ds_read_b64_tr_b16 v[204:205], v208 offset:7168
	ds_read_b64_tr_b16 v[206:207], v208 offset:7680
	s_waitcnt lgkmcnt(0)

.LBB0_974:
	s_and_b32 s8, s84, 1
	v_cndmask_b32_e64 v0, 0, 1, s[90:91]
	v_cmp_eq_u32_e32 vcc, s8, v0
	s_mov_b64 s[8:9], -1
	s_cbranch_vccz .LBB0_978
	s_cmpk_gt_u32 s84, 0xff
	s_cbranch_scc1 .LBB0_977
	v_add_u32_e32 v0, s29, v129
	s_mul_i32 s8, s84, 0xab
	s_bfe_u32 s8, s8, 0x70009
	s_waitcnt lgkmcnt(2)
	v_lshlrev_b32_e32 v48, 16, v176
	v_and_b32_e32 v49, 0xffff0000, v176
	v_lshlrev_b32_e32 v50, 16, v177
	v_and_b32_e32 v51, 0xffff0000, v177
	s_waitcnt lgkmcnt(1)
	v_lshlrev_b32_e32 v52, 16, v184
	v_and_b32_e32 v53, 0xffff0000, v184
	v_lshlrev_b32_e32 v54, 16, v185
	v_and_b32_e32 v55, 0xffff0000, v185
	s_waitcnt lgkmcnt(0)
	v_lshlrev_b32_e32 v56, 16, v192
	v_and_b32_e32 v57, 0xffff0000, v192
	v_lshlrev_b32_e32 v58, 16, v193
	v_and_b32_e32 v59, 0xffff0000, v193
	s_mul_i32 s8, s8, 3
	s_sub_i32 s8, s84, s8
	s_waitcnt lgkmcnt(2)
	v_lshlrev_b32_e32 v60, 16, v178
	v_and_b32_e32 v61, 0xffff0000, v178
	v_lshlrev_b32_e32 v62, 16, v179
	v_and_b32_e32 v63, 0xffff0000, v179
	s_waitcnt lgkmcnt(1)
	v_lshlrev_b32_e32 v64, 16, v186
	v_and_b32_e32 v65, 0xffff0000, v186
	v_lshlrev_b32_e32 v66, 16, v187
	v_and_b32_e32 v67, 0xffff0000, v187
	s_waitcnt lgkmcnt(0)
	v_lshlrev_b32_e32 v68, 16, v194
	v_and_b32_e32 v69, 0xffff0000, v194
	v_lshlrev_b32_e32 v70, 16, v195
	v_and_b32_e32 v71, 0xffff0000, v195
	s_and_b32 s8, s8, 0xff
	s_mulk_i32 s8, 0x5300
	s_add_i32 s8, s8, 0
	v_xor_b32_e32 v52, 0x80000000, v52
	v_mul_f32_e32 v56, v48, v56
	v_cvt_pk_bf16_f32 v52, v52, v56
	v_add_u32_e32 v56, s8, v127
	v_mul_f32_e32 v49, v48, v49
	v_mul_f32_e64 v48, v48, -v53
	s_waitcnt lgkmcnt(2)
	v_lshlrev_b32_e32 v72, 16, v180
	v_and_b32_e32 v73, 0xffff0000, v180
	v_lshlrev_b32_e32 v74, 16, v181
	v_and_b32_e32 v75, 0xffff0000, v181
	s_waitcnt lgkmcnt(1)
	v_lshlrev_b32_e32 v76, 16, v188
	v_and_b32_e32 v77, 0xffff0000, v188
	v_lshlrev_b32_e32 v78, 16, v189
	v_and_b32_e32 v79, 0xffff0000, v189
	s_waitcnt lgkmcnt(0)
	v_lshlrev_b32_e32 v80, 16, v196
	v_and_b32_e32 v81, 0xffff0000, v196
	v_lshlrev_b32_e32 v82, 16, v197
	v_and_b32_e32 v83, 0xffff0000, v197
	ds_write_b16 v56, v52
	ds_write_b16_d16_hi v56, v52 offset:2816
	v_mul_f32_e32 v52, v49, v57
	v_cvt_pk_bf16_f32 v48, v48, v52
	ds_write_b16 v56, v48 offset:176
	ds_write_b16_d16_hi v56, v48 offset:2992
	v_mul_f32_e32 v48, v49, v50
	v_mul_f32_e64 v49, v49, -v54
	v_mul_f32_e32 v50, v48, v58
	v_cvt_pk_bf16_f32 v49, v49, v50
	ds_write_b16 v56, v49 offset:352
	ds_write_b16_d16_hi v56, v49 offset:3168
	v_mul_f32_e32 v49, v48, v51
	v_mul_f32_e64 v48, v48, -v55
	v_mul_f32_e32 v50, v49, v59
	v_cvt_pk_bf16_f32 v48, v48, v50
	ds_write_b16 v56, v48 offset:528
	ds_write_b16_d16_hi v56, v48 offset:3344
	v_mul_f32_e32 v48, v49, v60
	v_mul_f32_e64 v49, v49, -v64
	v_mul_f32_e32 v50, v48, v68
	v_cvt_pk_bf16_f32 v49, v49, v50
	ds_write_b16 v56, v49 offset:704
	ds_write_b16_d16_hi v56, v49 offset:3520
	v_mul_f32_e32 v49, v48, v61
	v_mul_f32_e64 v48, v48, -v65
	v_mul_f32_e32 v50, v49, v69
	v_cvt_pk_bf16_f32 v48, v48, v50
	ds_write_b16 v56, v48 offset:880
	ds_write_b16_d16_hi v56, v48 offset:3696
	v_mul_f32_e32 v48, v49, v62
	v_mul_f32_e64 v49, v49, -v66
	v_mul_f32_e32 v50, v48, v70
	v_cvt_pk_bf16_f32 v49, v49, v50
	ds_write_b16 v56, v49 offset:1056
	ds_write_b16_d16_hi v56, v49 offset:3872
	v_mul_f32_e32 v49, v48, v63
	v_mul_f32_e64 v48, v48, -v67
	v_mul_f32_e32 v50, v49, v71
	v_cvt_pk_bf16_f32 v48, v48, v50
	ds_write_b16 v56, v48 offset:1232
	ds_write_b16_d16_hi v56, v48 offset:4048
	v_mul_f32_e32 v48, v49, v72
	v_mul_f32_e64 v49, v49, -v76
	v_mul_f32_e32 v50, v48, v80
	v_cvt_pk_bf16_f32 v49, v49, v50
	ds_write_b16 v56, v49 offset:1408
	ds_write_b16_d16_hi v56, v49 offset:4224
	v_mul_f32_e32 v49, v48, v73
	v_mul_f32_e64 v48, v48, -v77
	v_mul_f32_e32 v50, v49, v81
	v_cvt_pk_bf16_f32 v48, v48, v50
	ds_write_b16 v56, v48 offset:1584
	ds_write_b16_d16_hi v56, v48 offset:4400
	v_mul_f32_e32 v48, v49, v74
	v_mul_f32_e64 v49, v49, -v78
	v_mul_f32_e32 v50, v48, v82
	v_cvt_pk_bf16_f32 v49, v49, v50
	s_waitcnt lgkmcnt(14)
	v_lshlrev_b32_e32 v0, 16, v182
	ds_write_b16 v56, v49 offset:1760
	ds_write_b16_d16_hi v56, v49 offset:4576
	v_mul_f32_e32 v49, v48, v75
	v_mul_f32_e64 v48, v48, -v79
	v_and_b32_e32 v10, 0xffff0000, v182
	v_lshlrev_b32_e32 v85, 16, v190
	v_and_b32_e32 v12, 0xffff0000, v190
	v_lshlrev_b32_e32 v87, 16, v198
	v_mul_f32_e32 v50, v49, v83
	v_cvt_pk_bf16_f32 v48, v48, v50
	v_mul_f32_e32 v0, v49, v0
	v_and_b32_e32 v14, 0xffff0000, v198
	ds_write_b16 v56, v48 offset:1936
	ds_write_b16_d16_hi v56, v48 offset:4752
	v_mul_f32_e64 v48, v49, -v85
	v_mul_f32_e32 v49, v0, v87
	v_mul_f32_e32 v10, v0, v10
	v_mul_f32_e64 v0, v0, -v12
	v_lshlrev_b32_e32 v84, 16, v183
	v_lshlrev_b32_e32 v86, 16, v191
	v_cvt_pk_bf16_f32 v48, v48, v49
	v_mul_f32_e32 v12, v10, v14
	v_cvt_pk_bf16_f32 v0, v0, v12
	v_lshlrev_b32_e32 v88, 16, v199
	ds_write_b16 v56, v48 offset:2112
	ds_write_b16_d16_hi v56, v48 offset:4928
	ds_write_b16 v56, v0 offset:2288
	ds_write_b16_d16_hi v56, v0 offset:5104
	v_mul_f32_e32 v0, v10, v84
	v_mul_f32_e64 v10, v10, -v86
	v_and_b32_e32 v11, 0xffff0000, v183
	v_and_b32_e32 v13, 0xffff0000, v191
	v_mul_f32_e32 v12, v0, v88
	v_cvt_pk_bf16_f32 v10, v10, v12
	v_and_b32_e32 v15, 0xffff0000, v199
	ds_write_b16 v56, v10 offset:2464
	ds_write_b16_d16_hi v56, v10 offset:5280
	v_mul_f32_e32 v10, v0, v11
	v_mul_f32_e64 v0, v0, -v13
	v_mul_f32_e32 v11, v10, v15
	v_cvt_pk_bf16_f32 v0, v0, v11
	ds_write_b16 v56, v0 offset:2640
	ds_write_b16_d16_hi v56, v0 offset:5456
	v_add_u32_e32 v0, s8, v125
	ds_write_b32 v0, v10 offset:20992
	v_add_u32_e32 v0, s8, v134
	ds_write_b128 v0, v[200:203] offset:15360
	ds_write_b128 v0, v[204:207] offset:15376

.LBB0_978:
	s_andn2_b64 vcc, exec, s[8:9]
	s_cbranch_vccnz .LBB0_981
	s_cmpk_gt_u32 s84, 0xfe
	s_cbranch_scc1 .LBB0_981
	v_add_u32_e32 v2, s70, v126
	v_add_u32_e32 v0, 16, v2
	v_cndmask_b32_e64 v0, v115, v0, s[60:61]
	v_add_u32_e32 v2, 24, v2
	v_add_u32_e32 v0, s20, v0
	v_cndmask_b32_e64 v2, v117, v2, s[60:61]
	v_add_u32_e32 v2, s20, v2
	v_mov_b32_e32 v3, v1
	v_lshlrev_b64 v[4:5], 13, v[0:1]
	v_lshl_add_u64 v[14:15], v[118:119], 0, v[4:5]
	v_lshlrev_b64 v[4:5], 13, v[2:3]
	s_movk_i32 s12, 0x2800
	v_lshl_add_u64 v[56:57], v[118:119], 0, v[4:5]
	v_mad_u64_u32 v[4:5], s[8:9], v0, s12, v[120:121]
	v_mad_u64_u32 v[6:7], s[8:9], v2, s12, v[120:121]
	s_movk_i32 s8, 0x1000
	s_nop 0
	v_add_co_u32_e32 v60, vcc, s8, v14
	global_load_dwordx4 v[2:5], v[4:5], off nt
	s_nop 0
	global_load_dwordx4 v[6:9], v[6:7], off nt
	v_addc_co_u32_e32 v61, vcc, 0, v15, vcc
	global_load_dwordx4 v[10:13], v[60:61], off offset:2048 nt
	global_load_dwordx4 v[48:51], v[56:57], off nt
	global_load_dwordx4 v[52:55], v[14:15], off nt
	v_add_co_u32_e32 v14, vcc, s8, v56
	s_nop 1
	v_addc_co_u32_e32 v15, vcc, 0, v57, vcc
	global_load_dwordx4 v[56:59], v[14:15], off offset:2048 nt
	s_nop 0
	global_load_dwordx4 v[60:63], v[60:61], off nt
	s_nop 0
	global_load_dwordx4 v[64:67], v[14:15], off nt
	s_waitcnt vmcnt(0)
	s_waitcnt vmcnt(7)
	ds_write_b128 v151, v[2:5]
	s_waitcnt vmcnt(6)
	ds_write_b128 v151, v[6:9] offset:1024
	s_waitcnt vmcnt(3)
	ds_write_b128 v151, v[52:55] offset:4096
	ds_write_b128 v151, v[48:51] offset:5120
	ds_write_b128 v151, v[10:13] offset:2048
	s_waitcnt vmcnt(2)
	ds_write_b128 v151, v[56:59] offset:3072
	s_waitcnt vmcnt(1)
	ds_write_b128 v151, v[60:63] offset:6144
	s_waitcnt vmcnt(0)
	ds_write_b128 v151, v[64:67] offset:7168
	v_add_u32_e32 v208, s29, v129
	ds_read_b64_tr_b16 v[176:177], v208
	ds_read_b64_tr_b16 v[178:179], v208 offset:512
	ds_read_b64_tr_b16 v[180:181], v208 offset:1024
	ds_read_b64_tr_b16 v[182:183], v208 offset:1536
	ds_read_b64_tr_b16 v[184:185], v208 offset:2048
	ds_read_b64_tr_b16 v[186:187], v208 offset:2560
	ds_read_b64_tr_b16 v[188:189], v208 offset:3072
	ds_read_b64_tr_b16 v[190:191], v208 offset:3584
	ds_read_b64_tr_b16 v[192:193], v208 offset:4096
	ds_read_b64_tr_b16 v[194:195], v208 offset:4608
	ds_read_b64_tr_b16 v[196:197], v208 offset:5120
	ds_read_b64_tr_b16 v[198:199], v208 offset:5632
	ds_read_b64_tr_b16 v[200:201], v208 offset:6144
	ds_read_b64_tr_b16 v[202:203], v208 offset:6656
	ds_read_b64_tr_b16 v[204:205], v208 offset:7168
	ds_read_b64_tr_b16 v[206:207], v208 offset:7680
	s_waitcnt lgkmcnt(0)
